# grid barrier: non-leader workgroups poll the global generation word directly instead of the per-XCD relay word (one hop less on barrier exit), 11 barrier sites in the layer loop
# speedup vs baseline: 1.0006x; 1.0006x over previous
.LBB0_171:
	v_readlane_b32 s12, v253, 4
	v_readlane_b32 s13, v253, 5
	v_cvt_f32_u32_e32 v1, v2
	v_sub_u32_e32 v4, 0, v2
	v_rcp_iflag_f32_e32 v1, v1
	s_nop 1
	global_atomic_add v3, v113, v197, s[12:13] sc0
	v_mul_f32_e32 v1, 0x4f7ffffe, v1
	v_cvt_u32_f32_e32 v1, v1
	v_mul_lo_u32 v4, v4, v1
	v_mul_hi_u32 v4, v1, v4
	v_add_u32_e32 v1, v1, v4
	s_waitcnt vmcnt(0)
	v_mul_hi_u32 v1, v3, v1
	v_mul_lo_u32 v4, v1, v2
	v_sub_u32_e32 v4, v3, v4
	v_add_u32_e32 v5, 1, v1
	v_cmp_ge_u32_e32 vcc, v4, v2
	v_add_u32_e32 v3, 1, v3
	s_nop 0
	v_cndmask_b32_e32 v1, v1, v5, vcc
	v_sub_u32_e32 v5, v4, v2
	v_cndmask_b32_e32 v4, v4, v5, vcc
	v_add_u32_e32 v5, 1, v1
	v_cmp_ge_u32_e32 vcc, v4, v2
	s_nop 1
	v_cndmask_b32_e32 v1, v1, v5, vcc
	v_mul_lo_u32 v4, v2, v1
	v_add_u32_e32 v2, v4, v2
	v_cmp_ne_u32_e32 vcc, v3, v2
	s_and_saveexec_b64 s[12:13], vcc
	s_xor_b64 s[38:39], exec, s[12:13]
	s_cbranch_execz .LBB0_185
	v_readlane_b32 s12, v253, 10
	v_readlane_b32 s13, v253, 11
	s_waitcnt lgkmcnt(0)
	s_nop 3
	global_load_dword v0, v113, s[12:13] sc1
	s_waitcnt vmcnt(0)
	v_cmp_eq_u32_e32 vcc, v0, v1
	s_and_saveexec_b64 s[40:41], vcc
	s_cbranch_execz .LBB0_184
	s_mov_b32 s4, 1
	s_mov_b64 s[42:43], 0
	s_branch .LBB0_175

.LBB0_179:
	v_readlane_b32 s12, v253, 10
	v_readlane_b32 s13, v253, 11
	s_add_i32 s4, s4, 1
	s_mov_b64 s[50:51], -1
	s_nop 2
	global_load_dword v0, v113, s[12:13] sc1
	s_waitcnt vmcnt(0)
	v_cmp_ne_u32_e32 vcc, v0, v1
	s_orn2_b64 s[48:49], vcc, exec
	s_branch .LBB0_174

.LBB0_865:
	v_readlane_b32 s12, v253, 4
	v_readlane_b32 s13, v253, 5
	v_cvt_f32_u32_e32 v1, v2
	v_sub_u32_e32 v4, 0, v2
	v_rcp_iflag_f32_e32 v1, v1
	s_nop 1
	global_atomic_add v3, v113, v197, s[12:13] sc0
	v_mul_f32_e32 v1, 0x4f7ffffe, v1
	v_cvt_u32_f32_e32 v1, v1
	v_mul_lo_u32 v4, v4, v1
	v_mul_hi_u32 v4, v1, v4
	v_add_u32_e32 v1, v1, v4
	s_waitcnt vmcnt(0)
	v_mul_hi_u32 v1, v3, v1
	v_mul_lo_u32 v4, v1, v2
	v_sub_u32_e32 v4, v3, v4
	v_add_u32_e32 v5, 1, v1
	v_cmp_ge_u32_e32 vcc, v4, v2
	v_add_u32_e32 v3, 1, v3
	s_nop 0
	v_cndmask_b32_e32 v1, v1, v5, vcc
	v_sub_u32_e32 v5, v4, v2
	v_cndmask_b32_e32 v4, v4, v5, vcc
	v_add_u32_e32 v5, 1, v1
	v_cmp_ge_u32_e32 vcc, v4, v2
	s_nop 1
	v_cndmask_b32_e32 v1, v1, v5, vcc
	v_mul_lo_u32 v4, v2, v1
	v_add_u32_e32 v2, v4, v2
	v_cmp_ne_u32_e32 vcc, v3, v2
	s_and_saveexec_b64 s[12:13], vcc
	s_xor_b64 s[26:27], exec, s[12:13]
	s_cbranch_execz .LBB0_879
	v_readlane_b32 s12, v253, 10
	v_readlane_b32 s13, v253, 11
	s_waitcnt lgkmcnt(0)
	s_nop 3
	global_load_dword v0, v113, s[12:13] sc1
	s_waitcnt vmcnt(0)
	v_cmp_eq_u32_e32 vcc, v0, v1
	s_and_saveexec_b64 s[38:39], vcc
	s_cbranch_execz .LBB0_878
	s_mov_b32 s4, 1
	s_mov_b64 s[40:41], 0
	s_branch .LBB0_869

.LBB0_873:
	v_readlane_b32 s12, v253, 10
	v_readlane_b32 s13, v253, 11
	s_add_i32 s4, s4, 1
	s_mov_b64 s[48:49], -1
	s_nop 2
	global_load_dword v0, v113, s[12:13] sc1
	s_waitcnt vmcnt(0)
	v_cmp_ne_u32_e32 vcc, v0, v1
	s_orn2_b64 s[46:47], vcc, exec
	s_branch .LBB0_868

.LBB0_1035:
	v_readlane_b32 s12, v253, 4
	v_readlane_b32 s13, v253, 5
	v_cvt_f32_u32_e32 v1, v2
	v_sub_u32_e32 v4, 0, v2
	v_rcp_iflag_f32_e32 v1, v1
	s_nop 1
	global_atomic_add v3, v113, v197, s[12:13] sc0
	v_mul_f32_e32 v1, 0x4f7ffffe, v1
	v_cvt_u32_f32_e32 v1, v1
	v_mul_lo_u32 v4, v4, v1
	v_mul_hi_u32 v4, v1, v4
	v_add_u32_e32 v1, v1, v4
	s_waitcnt vmcnt(0)
	v_mul_hi_u32 v1, v3, v1
	v_mul_lo_u32 v4, v1, v2
	v_sub_u32_e32 v4, v3, v4
	v_add_u32_e32 v5, 1, v1
	v_cmp_ge_u32_e32 vcc, v4, v2
	v_add_u32_e32 v3, 1, v3
	s_nop 0
	v_cndmask_b32_e32 v1, v1, v5, vcc
	v_sub_u32_e32 v5, v4, v2
	v_cndmask_b32_e32 v4, v4, v5, vcc
	v_add_u32_e32 v5, 1, v1
	v_cmp_ge_u32_e32 vcc, v4, v2
	s_nop 1
	v_cndmask_b32_e32 v1, v1, v5, vcc
	v_mul_lo_u32 v4, v2, v1
	v_add_u32_e32 v2, v4, v2
	v_cmp_ne_u32_e32 vcc, v3, v2
	s_and_saveexec_b64 s[12:13], vcc
	s_xor_b64 s[26:27], exec, s[12:13]
	s_cbranch_execz .LBB0_1049
	v_readlane_b32 s12, v253, 10
	v_readlane_b32 s13, v253, 11
	s_waitcnt lgkmcnt(0)
	s_nop 3
	global_load_dword v0, v113, s[12:13] sc1
	s_waitcnt vmcnt(0)
	v_cmp_eq_u32_e32 vcc, v0, v1
	s_and_saveexec_b64 s[28:29], vcc
	s_cbranch_execz .LBB0_1048
	s_mov_b32 s4, 1
	s_mov_b64 s[38:39], 0
	s_branch .LBB0_1039

.LBB0_1043:
	v_readlane_b32 s12, v253, 10
	v_readlane_b32 s13, v253, 11
	s_add_i32 s4, s4, 1
	s_mov_b64 s[46:47], -1
	s_nop 2
	global_load_dword v0, v113, s[12:13] sc1
	s_waitcnt vmcnt(0)
	v_cmp_ne_u32_e32 vcc, v0, v1
	s_orn2_b64 s[42:43], vcc, exec
	s_branch .LBB0_1038

.LBB0_1190:
	v_readlane_b32 s12, v253, 4
	v_readlane_b32 s13, v253, 5
	v_cvt_f32_u32_e32 v1, v2
	v_sub_u32_e32 v4, 0, v2
	v_rcp_iflag_f32_e32 v1, v1
	s_nop 1
	global_atomic_add v3, v113, v197, s[12:13] sc0
	v_mul_f32_e32 v1, 0x4f7ffffe, v1
	v_cvt_u32_f32_e32 v1, v1
	v_mul_lo_u32 v4, v4, v1
	v_mul_hi_u32 v4, v1, v4
	v_add_u32_e32 v1, v1, v4
	s_waitcnt vmcnt(0)
	v_mul_hi_u32 v1, v3, v1
	v_mul_lo_u32 v4, v1, v2
	v_sub_u32_e32 v4, v3, v4
	v_add_u32_e32 v5, 1, v1
	v_cmp_ge_u32_e32 vcc, v4, v2
	v_add_u32_e32 v3, 1, v3
	s_nop 0
	v_cndmask_b32_e32 v1, v1, v5, vcc
	v_sub_u32_e32 v5, v4, v2
	v_cndmask_b32_e32 v4, v4, v5, vcc
	v_add_u32_e32 v5, 1, v1
	v_cmp_ge_u32_e32 vcc, v4, v2
	s_nop 1
	v_cndmask_b32_e32 v1, v1, v5, vcc
	v_mul_lo_u32 v4, v2, v1
	v_add_u32_e32 v2, v4, v2
	v_cmp_ne_u32_e32 vcc, v3, v2
	s_and_saveexec_b64 s[12:13], vcc
	s_xor_b64 s[26:27], exec, s[12:13]
	s_cbranch_execz .LBB0_1204
	v_readlane_b32 s12, v253, 10
	v_readlane_b32 s13, v253, 11
	s_waitcnt lgkmcnt(0)
	s_nop 3
	global_load_dword v0, v113, s[12:13] sc1
	s_waitcnt vmcnt(0)
	v_cmp_eq_u32_e32 vcc, v0, v1
	s_and_saveexec_b64 s[28:29], vcc
	s_cbranch_execz .LBB0_1203
	s_mov_b32 s2, 1
	s_mov_b64 s[38:39], 0
	s_branch .LBB0_1194

.LBB0_1198:
	v_readlane_b32 s12, v253, 10
	v_readlane_b32 s13, v253, 11
	s_add_i32 s2, s2, 1
	s_mov_b64 s[46:47], -1
	s_nop 2
	global_load_dword v0, v113, s[12:13] sc1
	s_waitcnt vmcnt(0)
	v_cmp_ne_u32_e32 vcc, v0, v1
	s_orn2_b64 s[42:43], vcc, exec
	s_branch .LBB0_1193
